# speedup vs baseline: 1.0082x; 1.0082x over previous
.Lepilogue:
	s_load_dword s26, s[8:9], 0x0
	s_cmpk_lt_u32 s19, 0x100
	s_cbranch_scc0 .LBB1_40
	s_bfe_u32 s2, s19, 0x10006
	s_lshl_b32 s3, s2, 9
	s_lshl_b32 s0, s2, 13
	s_add_u32 s0, s14, s0
	s_addc_u32 s1, s15, 0
	v_mov_b32_e32 v211, 0
	v_lshl_add_u64 v[6:7], s[0:1], 0, v[210:211]
	v_add_co_u32_e32 v2, vcc, 0x30000, v6
	s_mov_b64 s[0:1], 0x30000
	s_nop 0
	v_addc_co_u32_e32 v3, vcc, 0, v7, vcc
	global_load_dwordx4 v[2:5], v[2:3], off
	v_lshl_add_u64 v[8:9], v[6:7], 0, s[0:1]
	global_load_dwordx4 v[18:21], v[8:9], off offset:1024
	global_load_dwordx4 v[22:25], v[8:9], off offset:2048
	global_load_dwordx4 v[26:29], v[8:9], off offset:3072
	s_mov_b32 s0, 0x31000
	v_add_co_u32_e32 v46, vcc, s0, v6
	s_lshl_b32 s0, s19, 6
	s_nop 0
	v_addc_co_u32_e32 v47, vcc, 0, v7, vcc
	global_load_dwordx4 v[30:33], v[46:47], off
	s_and_b32 s0, s0, 0x2000
	v_or_b32_e32 v58, s0, v210
	ds_read_b128 v[6:9], v58
	ds_read_b128 v[34:37], v58 offset:1024
	global_load_dwordx4 v[38:41], v[46:47], off offset:1024
	v_lshl_or_b32 v62, s2, 7, v230
	s_and_b32 s0, s19, 0x80
	s_or_b32 s0, s3, s0
	s_waitcnt vmcnt(5) lgkmcnt(1)
	v_mfma_f32_32x32x16_bf16 v[2:17], v[2:5], v[6:9], 0
	s_waitcnt vmcnt(4) lgkmcnt(0)
	v_mfma_f32_32x32x16_bf16 v[2:17], v[18:21], v[34:37], v[2:17]
	global_load_dwordx4 v[18:21], v[46:47], off offset:2048
	ds_read_b128 v[34:37], v58 offset:2048
	ds_read_b128 v[42:45], v58 offset:3072
	ds_read_b128 v[50:53], v58 offset:5120
	s_waitcnt vmcnt(4) lgkmcnt(2)
	v_mfma_f32_32x32x16_bf16 v[2:17], v[22:25], v[34:37], v[2:17]
	global_load_dwordx4 v[22:25], v[46:47], off offset:3072
	global_load_dwordx4 v[34:37], v62, s[4:5]
	s_nop 0
	global_load_dwordx4 v[46:49], v62, s[4:5] offset:64
	s_waitcnt vmcnt(6) lgkmcnt(1)
	v_mfma_f32_32x32x16_bf16 v[2:17], v[26:29], v[42:45], v[2:17]
	ds_read_b128 v[42:45], v58 offset:4096
	global_load_dwordx4 v[26:29], v62, s[4:5] offset:32
	s_waitcnt vmcnt(6) lgkmcnt(0)
	v_mfma_f32_32x32x16_bf16 v[2:17], v[30:33], v[42:45], v[2:17]
	global_load_dwordx4 v[30:33], v62, s[4:5] offset:96
	global_load_dwordx4 v[42:45], v62, s[6:7]
	global_load_dwordx4 v[54:57], v62, s[6:7] offset:64
	s_waitcnt vmcnt(8)
	v_mfma_f32_32x32x16_bf16 v[2:17], v[38:41], v[50:53], v[2:17]
	global_load_dwordx4 v[38:41], v62, s[6:7] offset:32
	ds_read_b128 v[50:53], v58 offset:6144
	ds_read_b128 v[58:61], v58 offset:7168
	s_waitcnt vmcnt(8) lgkmcnt(1)
	v_mfma_f32_32x32x16_bf16 v[2:17], v[18:21], v[50:53], v[2:17]
	global_load_dwordx4 v[18:21], v62, s[6:7] offset:96
	v_lshlrev_b32_e32 v50, 2, v229
	s_waitcnt vmcnt(8) lgkmcnt(0)
	v_mfma_f32_32x32x16_bf16 v[2:17], v[22:25], v[58:61], v[2:17]
	s_waitcnt vmcnt(7)
	s_nop 10
	v_add_f32_e32 v2, v2, v34
	v_add_f32_e32 v3, v3, v35
	v_max_f32_e32 v2, 0, v2
	v_add_f32_e32 v4, v4, v36
	v_max_f32_e32 v3, 0, v3
	s_waitcnt vmcnt(3)
	v_fma_f32 v2, v2, v42, 0
	v_add_f32_e32 v5, v5, v37
	v_max_f32_e32 v4, 0, v4
	v_fmac_f32_e32 v2, v3, v43
	v_add_f32_e32 v6, v6, v26
	v_max_f32_e32 v5, 0, v5
	v_fmac_f32_e32 v2, v4, v44
	v_add_f32_e32 v7, v7, v27
	v_max_f32_e32 v6, 0, v6
	v_fmac_f32_e32 v2, v5, v45
	v_add_f32_e32 v8, v8, v28
	v_max_f32_e32 v7, 0, v7
	s_waitcnt vmcnt(1)
	v_fmac_f32_e32 v2, v6, v38
	v_add_f32_e32 v9, v9, v29
	v_max_f32_e32 v8, 0, v8
	v_fmac_f32_e32 v2, v7, v39
	v_add_f32_e32 v10, v10, v46
	v_max_f32_e32 v9, 0, v9
	v_fmac_f32_e32 v2, v8, v40
	v_add_f32_e32 v11, v11, v47
	v_max_f32_e32 v10, 0, v10
	v_fmac_f32_e32 v2, v9, v41
	v_add_f32_e32 v12, v12, v48
	v_max_f32_e32 v11, 0, v11
	v_fmac_f32_e32 v2, v10, v54
	v_add_f32_e32 v13, v13, v49
	v_max_f32_e32 v12, 0, v12
	v_fmac_f32_e32 v2, v11, v55
	v_add_f32_e32 v14, v14, v30
	v_max_f32_e32 v13, 0, v13
	v_fmac_f32_e32 v2, v12, v56
	v_add_f32_e32 v15, v15, v31
	v_max_f32_e32 v14, 0, v14
	v_fmac_f32_e32 v2, v13, v57
	v_add_f32_e32 v16, v16, v32
	v_max_f32_e32 v15, 0, v15
	v_add_f32_e32 v17, v17, v33
	v_max_f32_e32 v16, 0, v16
	v_max_f32_e32 v17, 0, v17
	v_add3_u32 v3, s0, v50, v228
	s_waitcnt vmcnt(0)
	v_fmac_f32_e32 v2, v14, v18
	v_fmac_f32_e32 v2, v15, v19
	v_fmac_f32_e32 v2, v16, v20
	v_fmac_f32_e32 v2, v17, v21
	ds_write_b32 v3, v2 offset:35904
.LBB1_40:
	v_cmp_gt_u32_e32 vcc, 64, v0
	s_waitcnt lgkmcnt(0)
	s_barrier
	s_and_saveexec_b64 s[0:1], vcc
	s_cbranch_execz .LBB1_42
	v_add_u32_e32 v1, 64, v1
	ds_read2st64_b32 v[2:3], v1 offset0:140 offset1:141
	ds_read2st64_b32 v[4:5], v1 offset0:142 offset1:143
	v_or_b32_e32 v0, s18, v0
	s_waitcnt lgkmcnt(0)
	v_add_f32_e32 v1, v2, v3
	v_add_f32_e32 v1, v1, v4
	v_add_f32_e32 v1, v1, v5
	v_add_f32_e32 v1, s26, v1
	v_mul_f32_e32 v1, 0xbfb8aa3b, v1
	v_exp_f32_e32 v1, v1
	s_nop 0
	v_add_f32_e32 v2, 1.0, v1
	v_div_scale_f32 v3, s[0:1], v2, v2, 1.0
	v_rcp_f32_e32 v4, v3
	v_div_scale_f32 v5, vcc, 1.0, v2, 1.0
	v_ashrrev_i32_e32 v1, 31, v0
	v_fma_f32 v6, -v3, v4, 1.0
	v_fmac_f32_e32 v4, v6, v4
	v_mul_f32_e32 v6, v5, v4
	v_fma_f32 v7, -v3, v6, v5
	v_fmac_f32_e32 v6, v7, v4
	v_fma_f32 v3, -v3, v6, v5
	v_div_fmas_f32 v3, v3, v4, v6
	v_div_fixup_f32 v2, v3, v2, 1.0
	v_lshl_add_u64 v[0:1], v[0:1], 2, s[10:11]
	global_store_dword v[0:1], v2, off
